# baseline (speedup 1.0000x reference)
.LBB1_12:
	s_mov_b32 s0, s44
	s_add_i32 s44, s44, 1
	s_cmp_ge_u32 s44, s42
	s_cselect_b64 s[22:23], -1, 0
	s_cmp_lt_u32 s44, s42
	s_cselect_b32 s2, s44, s0
	s_waitcnt vmcnt(0)
	s_lshl_b32 s0, s2, 4
	s_mov_b32 s1, s17
	s_mov_b32 m0, s43
	ds_read_b128 v[76:79], v119 offset:32768
	ds_read_b128 v[80:83], v119 offset:36864
	ds_read_b128 v[84:87], v120 offset:32768
	ds_read_b128 v[88:91], v120 offset:36864
	ds_read_b128 v[92:95], v121
	ds_read_b128 v[96:99], v121 offset:4096
	ds_read_b128 v[128:131], v122
	ds_read_b128 v[132:135], v122 offset:4096
	ds_read_b128 v[72:75], v123
	s_waitcnt lgkmcnt(0)
	v_lshl_add_u64 v[70:71], s[0:1], 2, v[2:3]
	global_load_lds_dword v[70:71], off
	ds_read_b128 v[156:159], v115
	ds_read_b128 v[160:163], v115 offset:1024
	ds_read_b128 v[164:167], v115 offset:2048
	v_cvt_pk_bf16_f32 v136, v76, v77
	v_cvt_pk_bf16_f32 v137, v78, v79
	v_cvt_pk_bf16_f32 v138, v84, v85
	v_cvt_pk_bf16_f32 v139, v86, v87
	v_cvt_pk_bf16_f32 v140, v92, v93
	v_cvt_pk_bf16_f32 v141, v94, v95
	v_cvt_pk_bf16_f32 v142, v128, v129
	v_cvt_pk_bf16_f32 v143, v130, v131
	v_cvt_pk_bf16_f32 v144, v80, v81
	v_cvt_pk_bf16_f32 v145, v82, v83
	v_cvt_pk_bf16_f32 v146, v88, v89
	v_cvt_pk_bf16_f32 v147, v90, v91
	v_cvt_pk_bf16_f32 v128, v96, v97
	v_cvt_pk_bf16_f32 v129, v98, v99
	v_cvt_pk_bf16_f32 v130, v132, v133
	v_cvt_pk_bf16_f32 v131, v134, v135
	s_lshl_b32 s0, s2, 13
	s_cmp_lt_u32 s44, s42
	s_cselect_b32 s0, s0, 0x1e848000
	s_mov_b32 s61, s0
	ds_read_b128 v[132:135], v115 offset:3072
	s_waitcnt lgkmcnt(3)
	v_mfma_f32_16x16x32_bf16 v[148:151], v[136:139], v[156:159], v[36:39]
	ds_read_b128 v[156:159], v115 offset:4096
	s_waitcnt lgkmcnt(3)
	v_mfma_f32_16x16x32_bf16 v[152:155], v[136:139], v[160:163], v[40:43]
	ds_read_b128 v[160:163], v115 offset:5120
	s_waitcnt lgkmcnt(3)
	v_mfma_f32_16x16x32_bf16 v[96:99], v[136:139], v[164:167], v[44:47]
	ds_read_b128 v[164:167], v115 offset:6144
	s_waitcnt lgkmcnt(3)
	v_mfma_f32_16x16x32_bf16 v[92:95], v[136:139], v[132:135], v[48:51]
	ds_read_b128 v[132:135], v115 offset:7168
	s_waitcnt lgkmcnt(3)
	v_mfma_f32_16x16x32_bf16 v[88:91], v[136:139], v[156:159], v[52:55]
	ds_read_b128 v[156:159], v115 offset:8192
	s_waitcnt lgkmcnt(3)
	v_mfma_f32_16x16x32_bf16 v[84:87], v[136:139], v[160:163], v[56:59]
	ds_read_b128 v[160:163], v115 offset:9216
	s_waitcnt lgkmcnt(3)
	v_mfma_f32_16x16x32_bf16 v[80:83], v[136:139], v[164:167], v[60:63]
	ds_read_b128 v[164:167], v115 offset:10240
	s_waitcnt lgkmcnt(3)
	v_mfma_f32_16x16x32_bf16 v[76:79], v[136:139], v[132:135], v[64:67]
	ds_read_b128 v[132:135], v115 offset:11264
	s_waitcnt lgkmcnt(3)
	v_mfma_f32_16x16x32_bf16 v[148:151], v[140:143], v[156:159], v[148:151]
	ds_read_b128 v[156:159], v115 offset:12288
	s_waitcnt lgkmcnt(3)
	v_mfma_f32_16x16x32_bf16 v[152:155], v[140:143], v[160:163], v[152:155]
	ds_read_b128 v[160:163], v115 offset:13312
	s_waitcnt lgkmcnt(3)
	v_mfma_f32_16x16x32_bf16 v[96:99], v[140:143], v[164:167], v[96:99]
	ds_read_b128 v[164:167], v115 offset:14336
	s_waitcnt lgkmcnt(3)
	v_mfma_f32_16x16x32_bf16 v[92:95], v[140:143], v[132:135], v[92:95]
	ds_read_b128 v[132:135], v115 offset:15360
	s_waitcnt lgkmcnt(3)
	v_mfma_f32_16x16x32_bf16 v[88:91], v[140:143], v[156:159], v[88:91]
	ds_read_b128 v[156:159], v115 offset:16384
	s_waitcnt lgkmcnt(3)
	v_mfma_f32_16x16x32_bf16 v[84:87], v[140:143], v[160:163], v[84:87]
	ds_read_b128 v[160:163], v115 offset:17408
	s_waitcnt lgkmcnt(3)
	v_mfma_f32_16x16x32_bf16 v[80:83], v[140:143], v[164:167], v[80:83]
	ds_read_b128 v[164:167], v115 offset:18432
	s_waitcnt lgkmcnt(3)
	v_mfma_f32_16x16x32_bf16 v[76:79], v[140:143], v[132:135], v[76:79]
	ds_read_b128 v[132:135], v115 offset:19456
	s_waitcnt lgkmcnt(3)
	s_mov_b32 m0, s47
	s_nop 0
	buffer_load_dwordx4 v113, s[12:15], s61 offen nt lds
	v_mfma_f32_16x16x32_bf16 v[148:151], v[144:147], v[156:159], v[148:151]
	ds_read_b128 v[156:159], v115 offset:20480
	s_waitcnt lgkmcnt(3)
	v_mfma_f32_16x16x32_bf16 v[152:155], v[144:147], v[160:163], v[152:155]
	ds_read_b128 v[160:163], v115 offset:21504
	s_waitcnt lgkmcnt(3)
	v_mfma_f32_16x16x32_bf16 v[96:99], v[144:147], v[164:167], v[96:99]
	ds_read_b128 v[164:167], v115 offset:22528
	s_waitcnt lgkmcnt(3)
	v_mfma_f32_16x16x32_bf16 v[92:95], v[144:147], v[132:135], v[92:95]
	ds_read_b128 v[132:135], v115 offset:23552
	s_waitcnt lgkmcnt(3)
	v_mfma_f32_16x16x32_bf16 v[88:91], v[144:147], v[156:159], v[88:91]
	ds_read_b128 v[156:159], v115 offset:24576
	s_waitcnt lgkmcnt(3)
	v_mfma_f32_16x16x32_bf16 v[84:87], v[144:147], v[160:163], v[84:87]
	ds_read_b128 v[160:163], v115 offset:25600
	s_waitcnt lgkmcnt(3)
	v_mfma_f32_16x16x32_bf16 v[80:83], v[144:147], v[164:167], v[80:83]
	ds_read_b128 v[164:167], v115 offset:26624
	s_waitcnt lgkmcnt(3)
	v_mfma_f32_16x16x32_bf16 v[76:79], v[144:147], v[132:135], v[76:79]
	ds_read_b128 v[132:135], v115 offset:27648
	s_waitcnt lgkmcnt(3)
	v_mfma_f32_16x16x32_bf16 v[148:151], v[128:131], v[156:159], v[148:151]
	ds_read_b128 v[156:159], v115 offset:28672
	s_waitcnt lgkmcnt(3)
	v_mfma_f32_16x16x32_bf16 v[152:155], v[128:131], v[160:163], v[152:155]
	ds_read_b128 v[160:163], v115 offset:29696
	s_waitcnt lgkmcnt(3)
	v_mfma_f32_16x16x32_bf16 v[96:99], v[128:131], v[164:167], v[96:99]
	ds_read_b128 v[164:167], v115 offset:30720
	s_waitcnt lgkmcnt(3)
	v_mfma_f32_16x16x32_bf16 v[92:95], v[128:131], v[132:135], v[92:95]
	ds_read_b128 v[132:135], v115 offset:31744
	s_waitcnt lgkmcnt(3)
	v_mfma_f32_16x16x32_bf16 v[88:91], v[128:131], v[156:159], v[88:91]
	s_waitcnt lgkmcnt(2)
	v_mfma_f32_16x16x32_bf16 v[84:87], v[128:131], v[160:163], v[84:87]
	s_waitcnt lgkmcnt(1)
	v_mfma_f32_16x16x32_bf16 v[80:83], v[128:131], v[164:167], v[80:83]
	s_waitcnt lgkmcnt(0)
	v_mfma_f32_16x16x32_bf16 v[76:79], v[128:131], v[132:135], v[76:79]
	s_or_b32 s62, s61, 0x800
	s_mov_b32 m0, s48
	s_nop 0
	buffer_load_dwordx4 v113, s[12:15], s62 offen nt lds
	ds_read2_b32 v[136:137], v114 offset0:128 offset1:144
	ds_read2_b32 v[138:139], v125 offset1:16
	ds_read2_b32 v[140:141], v114 offset0:160 offset1:176
	ds_read2_b32 v[142:143], v125 offset0:32 offset1:48
	ds_read2_b32 v[144:145], v114 offset0:192 offset1:208
	ds_read2_b32 v[146:147], v125 offset0:64 offset1:80
	ds_read2_b32 v[156:157], v114 offset0:224 offset1:240
	ds_read2_b32 v[158:159], v125 offset0:96 offset1:112
	v_fma_f32 v70, v149, v149, 0
	v_fmac_f32_e32 v70, v153, v153
	v_fmac_f32_e32 v70, v97, v97
	v_fmac_f32_e32 v70, v93, v93
	v_fmac_f32_e32 v70, v89, v89
	v_fmac_f32_e32 v70, v85, v85
	v_fmac_f32_e32 v70, v81, v81
	v_fmac_f32_e32 v70, v77, v77
	v_fma_f32 v68, v148, v148, 0
	v_fmac_f32_e32 v68, v152, v152
	v_add_f32_dpp v70, v70, v70 quad_perm:[1,0,3,2] row_mask:0xf bank_mask:0xf bound_ctrl:1
	v_fmac_f32_e32 v68, v96, v96
	v_fmac_f32_e32 v68, v92, v92
	v_add_f32_dpp v70, v70, v70 quad_perm:[2,3,0,1] row_mask:0xf bank_mask:0xf bound_ctrl:1
	v_fmac_f32_e32 v68, v88, v88
	v_fmac_f32_e32 v68, v84, v84
	v_add_f32_dpp v70, v70, v70 row_half_mirror row_mask:0xf bank_mask:0xf bound_ctrl:1
	v_fmac_f32_e32 v68, v80, v80
	v_fmac_f32_e32 v68, v76, v76
	v_add_f32_dpp v70, v70, v70 row_mirror row_mask:0xf bank_mask:0xf bound_ctrl:1
	v_fmamk_f32 v70, v70, 0x3c000000, v124
	s_or_b32 s62, s61, 0x1000
	s_mov_b32 m0, s49
	s_nop 0
	buffer_load_dwordx4 v113, s[12:15], s62 offen nt lds
	v_rsq_f32_e32 v127, v70
	v_fma_f32 v70, v150, v150, 0
	v_fmac_f32_e32 v70, v154, v154
	v_fmac_f32_e32 v70, v98, v98
	v_fmac_f32_e32 v70, v94, v94
	v_fmac_f32_e32 v70, v90, v90
	v_fmac_f32_e32 v70, v86, v86
	v_fmac_f32_e32 v70, v82, v82
	v_fmac_f32_e32 v70, v78, v78
	v_add_f32_dpp v68, v68, v68 quad_perm:[1,0,3,2] row_mask:0xf bank_mask:0xf bound_ctrl:1
	v_mul_f32_e32 v131, v127, v149
	v_add_f32_dpp v70, v70, v70 quad_perm:[1,0,3,2] row_mask:0xf bank_mask:0xf bound_ctrl:1
	v_add_f32_dpp v68, v68, v68 quad_perm:[2,3,0,1] row_mask:0xf bank_mask:0xf bound_ctrl:1
	v_mul_f32_e32 v81, v127, v81
	v_add_f32_dpp v70, v70, v70 quad_perm:[2,3,0,1] row_mask:0xf bank_mask:0xf bound_ctrl:1
	v_add_f32_dpp v68, v68, v68 row_half_mirror row_mask:0xf bank_mask:0xf bound_ctrl:1
	v_cmp_gt_u32_e64 s[0:1], s55, v72
	v_add_f32_dpp v70, v70, v70 row_half_mirror row_mask:0xf bank_mask:0xf bound_ctrl:1
	v_add_f32_dpp v68, v68, v68 row_mirror row_mask:0xf bank_mask:0xf bound_ctrl:1
	v_fmamk_f32 v68, v68, 0x3c000000, v124
	v_add_f32_dpp v70, v70, v70 row_mirror row_mask:0xf bank_mask:0xf bound_ctrl:1
	v_fmamk_f32 v70, v70, 0x3c000000, v124
	v_rsq_f32_e32 v130, v70
	v_fma_f32 v70, v151, v151, 0
	v_fmac_f32_e32 v70, v155, v155
	v_fmac_f32_e32 v70, v99, v99
	v_fmac_f32_e32 v70, v95, v95
	v_fmac_f32_e32 v70, v91, v91
	v_fmac_f32_e32 v70, v87, v87
	v_fmac_f32_e32 v70, v83, v83
	v_fmac_f32_e32 v70, v79, v79
	v_rsq_f32_e32 v68, v68
	v_mul_f32_e32 v98, v130, v98
	v_add_f32_dpp v70, v70, v70 quad_perm:[1,0,3,2] row_mask:0xf bank_mask:0xf bound_ctrl:1
	v_mul_f32_e32 v90, v130, v90
	v_mul_f32_e32 v111, v68, v148
	v_add_f32_dpp v110, v70, v70 quad_perm:[2,3,0,1] row_mask:0xf bank_mask:0xf bound_ctrl:1
	s_nop 1
	v_add_f32_dpp v110, v110, v110 row_half_mirror row_mask:0xf bank_mask:0xf bound_ctrl:1
	v_mul_f32_e32 v96, v68, v96
	v_mul_f32_e32 v92, v68, v92
	v_add_f32_dpp v110, v110, v110 row_mirror row_mask:0xf bank_mask:0xf bound_ctrl:1
	v_fmamk_f32 v110, v110, 0x3c000000, v124
	s_waitcnt lgkmcnt(0)
	s_or_b32 s62, s61, 0x1800
	s_mov_b32 m0, s50
	s_nop 0
	buffer_load_dwordx4 v113, s[12:15], s62 offen nt lds
	v_fma_f32 v111, v111, v136, v138
	v_fma_f32 v131, v131, v136, v138
	v_exp_f32_e32 v111, v111
	v_exp_f32_e32 v131, v131
	v_rsq_f32_e32 v132, v110
	v_mul_f32_e32 v88, v68, v88
	v_add_f32_e32 v110, 1.0, v111
	v_add_f32_e32 v111, 1.0, v131
	v_mul_f32_e32 v131, v130, v150
	v_mul_f32_e32 v133, v132, v151
	v_fma_f32 v131, v131, v136, v138
	v_fma_f32 v70, v133, v136, v138
	v_exp_f32_e32 v131, v131
	v_exp_f32_e32 v70, v70
	v_rcp_f32_e32 v110, v110
	v_rcp_f32_e32 v111, v111
	v_add_f32_e32 v128, 1.0, v131
	v_add_f32_e32 v70, 1.0, v70
	v_rcp_f32_e32 v128, v128
	v_rcp_f32_e32 v70, v70
	v_mul_f32_e32 v131, v68, v152
	v_fma_f32 v131, v131, v137, v139
	v_cvt_pk_bf16_f32 v110, v110, v111
	v_cvt_pk_bf16_f32 v111, v128, v70
	v_mul_f32_e32 v128, v127, v153
	v_exp_f32_e32 v131, v131
	v_fma_f32 v128, v128, v137, v139
	v_exp_f32_e32 v128, v128
	v_mul_f32_e32 v99, v132, v99
	v_add_f32_e32 v70, 1.0, v131
	v_rcp_f32_e32 v133, v70
	v_add_f32_e32 v70, 1.0, v128
	v_mul_f32_e32 v131, v130, v154
	v_rcp_f32_e32 v134, v70
	v_mul_f32_e32 v70, v132, v155
	v_fma_f32 v131, v131, v137, v139
	v_fma_f32 v129, v70, v137, v139
	v_exp_f32_e32 v135, v129
	v_exp_f32_e32 v131, v131
	v_mul_f32_e32 v91, v132, v91
	v_add_f32_e32 v135, 1.0, v135
	v_rcp_f32_e32 v135, v135
	s_or_b32 s62, s61, 0x100
	s_mov_b32 m0, s51
	s_nop 0
	buffer_load_dwordx4 v113, s[12:15], s62 offen nt lds
	v_fma_f32 v96, v96, v140, v142
	v_exp_f32_e32 v136, v96
	v_mul_f32_e32 v96, v127, v97
	v_fma_f32 v96, v96, v140, v142
	v_exp_f32_e32 v97, v96
	v_fma_f32 v98, v98, v140, v142
	v_fma_f32 v70, v99, v140, v142
	v_exp_f32_e32 v98, v98
	v_exp_f32_e32 v70, v70
	v_add_f32_e32 v97, 1.0, v97
	v_cvt_pk_bf16_f32 v96, v133, v134
	v_add_f32_e32 v133, 1.0, v136
	v_rcp_f32_e32 v99, v97
	v_add_f32_e32 v97, 1.0, v98
	v_add_f32_e32 v70, 1.0, v70
	v_fma_f32 v92, v92, v141, v143
	v_rcp_f32_e32 v133, v133
	v_rcp_f32_e32 v128, v97
	v_rcp_f32_e32 v70, v70
	v_exp_f32_e32 v92, v92
	v_cvt_pk_bf16_f32 v98, v133, v99
	v_add_f32_e32 v131, 1.0, v131
	v_cvt_pk_bf16_f32 v99, v128, v70
	v_add_f32_e32 v70, 1.0, v92
	v_mul_f32_e32 v92, v127, v93
	v_fma_f32 v92, v92, v141, v143
	v_exp_f32_e32 v92, v92
	v_mul_f32_e32 v93, v130, v94
	v_fma_f32 v93, v93, v141, v143
	v_rcp_f32_e32 v131, v131
	v_exp_f32_e32 v93, v93
	v_rcp_f32_e32 v94, v70
	v_add_f32_e32 v70, 1.0, v92
	v_rcp_f32_e32 v128, v70
	v_mul_f32_e32 v70, v132, v95
	v_cvt_pk_bf16_f32 v97, v131, v135
	v_add_f32_e32 v131, 1.0, v93
	v_fma_f32 v129, v70, v141, v143
	v_exp_f32_e32 v95, v129
	v_rcp_f32_e32 v129, v131
	v_mul_f32_e32 v84, v68, v84
	v_mul_f32_e32 v80, v68, v80
	s_or_b32 s62, s61, 0x900
	s_mov_b32 m0, s52
	s_nop 0
	buffer_load_dwordx4 v113, s[12:15], s62 offen nt lds
	v_fma_f32 v88, v88, v144, v146
	v_exp_f32_e32 v131, v88
	v_mul_f32_e32 v88, v127, v89
	v_fma_f32 v88, v88, v144, v146
	v_exp_f32_e32 v89, v88
	v_fma_f32 v90, v90, v144, v146
	v_fma_f32 v70, v91, v144, v146
	v_exp_f32_e32 v90, v90
	v_exp_f32_e32 v70, v70
	v_add_f32_e32 v89, 1.0, v89
	v_cvt_pk_bf16_f32 v88, v94, v128
	v_add_f32_e32 v94, 1.0, v131
	v_rcp_f32_e32 v91, v89
	v_add_f32_e32 v89, 1.0, v90
	v_add_f32_e32 v70, 1.0, v70
	v_fma_f32 v84, v84, v145, v147
	v_rcp_f32_e32 v94, v94
	v_rcp_f32_e32 v92, v89
	v_rcp_f32_e32 v70, v70
	v_exp_f32_e32 v84, v84
	v_cvt_pk_bf16_f32 v90, v94, v91
	v_mul_f32_e32 v68, v68, v76
	v_cvt_pk_bf16_f32 v91, v92, v70
	v_add_f32_e32 v70, 1.0, v84
	v_mul_f32_e32 v84, v127, v85
	v_fma_f32 v84, v84, v145, v147
	v_mul_f32_e32 v85, v130, v86
	v_exp_f32_e32 v84, v84
	v_fma_f32 v85, v85, v145, v147
	v_exp_f32_e32 v85, v85
	v_rcp_f32_e32 v92, v70
	v_add_f32_e32 v70, 1.0, v84
	v_rcp_f32_e32 v84, v70
	v_add_f32_e32 v70, 1.0, v85
	v_mul_f32_e32 v85, v132, v87
	v_fma_f32 v93, v85, v145, v147
	v_exp_f32_e32 v85, v93
	v_rcp_f32_e32 v93, v70
	v_mul_f32_e32 v76, v127, v77
	v_mul_f32_e32 v82, v130, v82
	v_mul_f32_e32 v83, v132, v83
	v_mul_f32_e32 v77, v130, v78
	s_or_b32 s62, s61, 0x1100
	s_mov_b32 m0, s53
	s_nop 0
	buffer_load_dwordx4 v113, s[12:15], s62 offen nt lds
	v_fma_f32 v76, v76, v157, v159
	v_mul_f32_e32 v78, v132, v79
	v_fma_f32 v80, v80, v156, v158
	v_fma_f32 v81, v81, v156, v158
	v_fma_f32 v82, v82, v156, v158
	v_fma_f32 v70, v83, v156, v158
	v_fma_f32 v68, v68, v157, v159
	v_exp_f32_e32 v76, v76
	v_fma_f32 v77, v77, v157, v159
	v_fma_f32 v87, v78, v157, v159
	v_exp_f32_e32 v82, v82
	v_exp_f32_e32 v70, v70
	v_exp_f32_e32 v68, v68
	v_exp_f32_e32 v77, v77
	v_exp_f32_e32 v71, v87
	v_add_f32_e32 v76, 1.0, v76
	v_add_f32_e32 v82, 1.0, v82
	v_add_f32_e32 v70, 1.0, v70
	v_add_f32_e32 v68, 1.0, v68
	v_rcp_f32_e32 v78, v76
	v_add_f32_e32 v76, 1.0, v77
	v_add_f32_e32 v71, 1.0, v71
	v_rcp_f32_e32 v82, v82
	v_rcp_f32_e32 v70, v70
	v_rcp_f32_e32 v68, v68
	v_rcp_f32_e32 v79, v76
	v_rcp_f32_e32 v71, v71
	v_exp_f32_e32 v80, v80
	v_exp_f32_e32 v81, v81
	v_cvt_pk_bf16_f32 v77, v82, v70
	v_cvt_pk_bf16_f32 v78, v68, v78
	v_cvt_pk_bf16_f32 v79, v79, v71
	v_subrev_u32_e32 v68, s16, v72
	v_subrev_u32_e32 v70, s16, v73
	v_subrev_u32_e32 v71, s16, v74
	v_add_f32_e32 v95, 1.0, v95
	v_add_f32_e32 v85, 1.0, v85
	v_add_f32_e32 v80, 1.0, v80
	v_add_f32_e32 v81, 1.0, v81
	s_or_b32 s62, s61, 0x1900
	s_mov_b32 m0, s54
	s_nop 0
	buffer_load_dwordx4 v113, s[12:15], s62 offen nt lds
	v_max3_u32 v68, v68, v70, v71
	v_subrev_u32_e32 v70, s16, v75
	v_rcp_f32_e32 v95, v95
	v_rcp_f32_e32 v85, v85
	v_rcp_f32_e32 v80, v80
	v_rcp_f32_e32 v81, v81
	v_max_u32_e32 v68, v68, v70
	v_cmp_gt_u32_e32 vcc, 16, v68
	s_cmp_eq_u64 vcc, -1
	s_cselect_b64 s[24:25], -1, 0
	s_cmp_lg_u64 vcc, -1
	v_cvt_pk_bf16_f32 v89, v129, v95
	v_cvt_pk_bf16_f32 v84, v92, v84
	v_cvt_pk_bf16_f32 v85, v93, v85
	v_cvt_pk_bf16_f32 v76, v80, v81
	s_cselect_b64 s[26:27], -1, 0
	v_cmp_gt_u32_e64 s[2:3], s55, v73
	v_cmp_gt_u32_e64 s[4:5], s55, v74
	v_cmp_gt_u32_e64 s[6:7], s55, v75
	s_mov_b32 s8, 0
	s_branch .LBB1_14
